# baseline (speedup 1.0000x reference)
_Z11k_proj_mfmaPKDF16_PKDv8_DF16_PKfPfPS1_S6_PhS6_PDF16_:
	v_readfirstlane_b32 s21, v0
	s_lshr_b32 s20, s21, 6
	s_and_b32 s24, s2, 3
	s_cmp_lg_u32 s24, 0
	s_cselect_b64 s[8:9], -1, 0
	s_cmp_eq_u32 s24, 2
	s_cselect_b32 s3, 28, 40
	s_cselect_b32 s4, 40, 50
	s_cmp_eq_u32 s24, 1
	s_cselect_b32 s3, 18, s3
	s_cselect_b32 s10, 28, s4
	s_cmp_eq_u32 s24, 0
	s_cselect_b64 s[4:5], -1, 0
	s_load_dwordx2 s[16:17], s[0:1], 0x8
	s_load_dwordx16 s[36:51], s[0:1], 0x0
	s_load_dwordx2 s[52:53], s[0:1], 0x40
	s_and_b64 s[6:7], s[4:5], exec
	s_cselect_b32 s26, 0, s3
	s_cselect_b32 s3, 18, s10
	s_add_i32 s27, s20, s26
	s_cmp_lt_u32 s27, s3
	s_cselect_b64 s[14:15], -1, 0
	s_cmp_ge_u32 s27, s3
	v_and_b32_e32 v146, 63, v0
	s_cbranch_scc1 .LBB2_2
	s_mul_i32 s6, s27, 0x140
	v_or_b32_e32 v2, s6, v146
	v_mov_b32_e32 v3, 0
	s_waitcnt lgkmcnt(0)
	v_lshl_add_u64 v[4:5], v[2:3], 4, s[16:17]
	s_addk_i32 s6, 0x100
	global_load_dwordx4 v[106:109], v[4:5], off
	global_load_dwordx4 v[114:117], v[4:5], off offset:1024
	global_load_dwordx4 v[126:129], v[4:5], off offset:2048
	global_load_dwordx4 v[134:137], v[4:5], off offset:3072
	v_or_b32_e32 v2, s6, v146
	v_lshl_add_u64 v[2:3], v[2:3], 4, s[16:17]
	global_load_dwordx4 v[138:141], v[2:3], off
.LBB2_2:
	s_mov_b64 s[6:7], s[36:37]
	s_add_i32 s28, s27, 8
	s_cmp_lt_u32 s28, s3
	s_cselect_b64 s[12:13], -1, 0
	s_cmp_ge_u32 s28, s3
	s_cbranch_scc1 .LBB2_4
	s_mul_i32 s10, s28, 0x140
	v_or_b32_e32 v2, s10, v146
	v_mov_b32_e32 v3, 0
	s_waitcnt lgkmcnt(0)
	v_lshl_add_u64 v[4:5], v[2:3], 4, s[16:17]
	s_addk_i32 s10, 0x100
	global_load_dwordx4 v[22:25], v[4:5], off
	global_load_dwordx4 v[26:29], v[4:5], off offset:1024
	global_load_dwordx4 v[30:33], v[4:5], off offset:2048
	global_load_dwordx4 v[34:37], v[4:5], off offset:3072
	v_or_b32_e32 v2, s10, v146
	v_lshl_add_u64 v[2:3], v[2:3], 4, s[16:17]
	global_load_dwordx4 v[38:41], v[2:3], off

.LBB2_8:
	s_or_b64 exec, exec, s[2:3]
	s_mov_b64 s[16:17], s[40:41]
	v_or_b32_e32 v56, 0x400, v0
	s_movk_i32 s2, 0x500
	s_and_b32 s23, s18, 0xffffffc
	v_cmp_gt_u32_e64 s[2:3], s2, v56
	s_and_saveexec_b64 s[18:19], s[2:3]
	s_cbranch_execz .LBB2_10
	v_mul_u32_u24_e32 v50, 0xccd, v56
	s_movk_i32 s29, 0xffec
	v_mul_i32_i24_sdwa v52, v50, s29 dst_sel:DWORD dst_unused:UNUSED_PAD src0_sel:WORD_1 src1_sel:DWORD
	v_add_u32_sdwa v53, s25, v50 dst_sel:DWORD dst_unused:UNUSED_PAD src0_sel:DWORD src1_sel:WORD_1
	s_movk_i32 s29, 0x140
	v_mov_b64_e32 v[50:51], s[6:7]
	v_add_lshl_u32 v52, v52, v56, 3
	v_mad_u64_u32 v[50:51], s[6:7], v53, s29, v[50:51]
	v_ashrrev_i32_e32 v53, 31, v52
	v_lshl_add_u64 v[50:51], v[52:53], 1, v[50:51]
	global_load_dwordx4 v[50:53], v[50:51], off

.LBB2_113:
	s_cmpk_lt_u32 s21, 0x100
	s_mov_b64 s[2:3], -1
	s_cselect_b64 s[10:11], -1, 0
	s_and_b64 vcc, exec, s[8:9]
	s_waitcnt lgkmcnt(0)
	s_barrier
	s_cbranch_vccz .LBB2_141
	s_cmp_lt_i32 s24, 2
	s_cbranch_scc1 .LBB2_137
	s_cmp_eq_u32 s24, 2
	s_cbranch_scc1 .LBB2_119
	s_mov_b64 s[8:9], s[52:53]
	s_mov_b64 s[2:3], 0
	s_movk_i32 s4, 0xffec
	s_movk_i32 s5, 0x310
	s_movk_i32 s6, 0x140
	s_waitcnt lgkmcnt(0)
	v_mov_b64_e32 v[2:3], s[8:9]
	s_movk_i32 s7, 0x2ff
	v_mov_b32_e32 v4, v0

.LBB2_119:
	s_and_b64 vcc, exec, s[2:3]
	s_cbranch_vccz .LBB2_136
	s_mov_b64 s[6:7], s[48:49]
	v_cndmask_b32_e64 v2, 0, 1, s[10:11]
	v_cmp_ne_u32_e64 s[2:3], 1, v2
	s_andn2_b64 vcc, exec, s[10:11]
	v_mov_b32_e32 v2, 0
	s_cbranch_vccnz .LBB2_122
	v_and_b32_e32 v3, 3, v0
	v_lshrrev_b32_e32 v2, 2, v0
	v_mul_u32_u24_e32 v3, 0xa0, v3
	s_movk_i32 s4, 0x310
	v_mad_u32_u24 v22, v2, s4, v3
	ds_read_b128 v[2:5], v22
	ds_read_b128 v[8:11], v22 offset:16
	v_lshl_add_u32 v6, s22, 8, v0
	v_lshrrev_b32_e32 v6, 5, v6
	v_mov_b32_e32 v7, 0
	s_waitcnt lgkmcnt(0)
	v_cvt_f16_f32_e32 v14, v3
	v_lshlrev_b64 v[12:13], 12, v[6:7]
	v_cvt_f16_f32_e32 v6, v2
	v_cvt_f16_f32_e32 v25, v4
	v_cvt_f32_f16_e32 v24, v14
	v_lshl_add_u64 v[20:21], s[6:7], 0, v[12:13]
	ds_read_b128 v[12:15], v22 offset:32
	ds_read_b128 v[16:19], v22 offset:48
	v_cvt_f16_f32_e32 v26, v9
	v_mul_f32_e32 v24, v24, v24
	v_fma_mix_f32 v6, v6, v6, v24 op_sel_hi:[1,1,0]
	v_cvt_f16_f32_e32 v24, v5
	v_fma_mix_f32 v6, v25, v25, v6 op_sel_hi:[1,1,0]
	v_cvt_f16_f32_e32 v25, v8
	v_cvt_f16_f32_e32 v27, v10
	v_fma_mix_f32 v6, v24, v24, v6 op_sel_hi:[1,1,0]
	v_cvt_f16_f32_e32 v24, v11
	v_fma_mix_f32 v6, v25, v25, v6 op_sel_hi:[1,1,0]
	v_cvt_pk_f16_f32 v11, v10, v11
	v_cvt_pk_f16_f32 v10, v8, v9
	v_cvt_pk_f16_f32 v8, v2, v3
	s_waitcnt lgkmcnt(1)
	v_cvt_f16_f32_e32 v3, v12
	v_fma_mix_f32 v6, v26, v26, v6 op_sel_hi:[1,1,0]
	v_cvt_pk_f16_f32 v9, v4, v5
	v_cvt_f16_f32_e32 v4, v13
	v_fma_mix_f32 v6, v27, v27, v6 op_sel_hi:[1,1,0]
	v_cvt_f16_f32_e32 v5, v14
	v_fma_mix_f32 v2, v24, v24, v6 op_sel_hi:[1,1,0]
	v_and_b32_e32 v23, 31, v0
	v_fma_mix_f32 v2, v3, v3, v2 op_sel_hi:[1,1,0]
	v_cvt_f16_f32_e32 v3, v15
	v_lshlrev_b32_e32 v6, 4, v23
	v_fma_mix_f32 v2, v4, v4, v2 op_sel_hi:[1,1,0]
	s_waitcnt lgkmcnt(0)
	v_cvt_f16_f32_e32 v4, v16
	v_lshl_add_u64 v[20:21], v[20:21], 0, v[6:7]
	v_fma_mix_f32 v2, v5, v5, v2 op_sel_hi:[1,1,0]
	v_cvt_f16_f32_e32 v5, v17
	global_store_dwordx4 v[20:21], v[8:11], off
	v_cvt_f16_f32_e32 v6, v18
	ds_read_b128 v[8:11], v22 offset:64
	v_fma_mix_f32 v2, v3, v3, v2 op_sel_hi:[1,1,0]
	v_cvt_f16_f32_e32 v23, v19
	v_fma_mix_f32 v2, v4, v4, v2 op_sel_hi:[1,1,0]
	v_cvt_pk_f16_f32 v3, v14, v15
	v_fma_mix_f32 v2, v5, v5, v2 op_sel_hi:[1,1,0]
	v_cvt_pk_f16_f32 v4, v16, v17
	v_fma_mix_f32 v6, v6, v6, v2 op_sel_hi:[1,1,0]
	v_cvt_pk_f16_f32 v2, v12, v13
	ds_read_b128 v[12:15], v22 offset:80
	s_waitcnt lgkmcnt(1)
	v_cvt_f16_f32_e32 v16, v8
	v_cvt_f16_f32_e32 v17, v9
	v_cvt_pk_f16_f32 v5, v18, v19
	v_cvt_f16_f32_e32 v18, v10
	v_fma_mix_f32 v6, v23, v23, v6 op_sel_hi:[1,1,0]
	global_store_dwordx4 v[20:21], v[2:5], off offset:512
	s_mov_b32 s4, 0xf800000
	s_nop 0
	v_cvt_f16_f32_e32 v3, v11
	v_fma_mix_f32 v2, v16, v16, v6 op_sel_hi:[1,1,0]
	s_waitcnt lgkmcnt(0)
	v_cvt_f16_f32_e32 v4, v12
	v_fma_mix_f32 v2, v17, v17, v2 op_sel_hi:[1,1,0]
	v_cvt_f16_f32_e32 v5, v13
	v_fma_mix_f32 v2, v18, v18, v2 op_sel_hi:[1,1,0]
	v_cvt_f16_f32_e32 v6, v14
	v_fma_mix_f32 v2, v3, v3, v2 op_sel_hi:[1,1,0]
	v_cvt_f16_f32_e32 v16, v15
	v_fma_mix_f32 v2, v4, v4, v2 op_sel_hi:[1,1,0]
	v_cvt_pk_f16_f32 v4, v12, v13
	v_fma_mix_f32 v2, v5, v5, v2 op_sel_hi:[1,1,0]
	v_cvt_pk_f16_f32 v5, v14, v15
	ds_read_b128 v[12:15], v22 offset:96
	v_fma_mix_f32 v6, v6, v6, v2 op_sel_hi:[1,1,0]
	v_cvt_pk_f16_f32 v3, v10, v11
	v_cvt_pk_f16_f32 v2, v8, v9
	v_fma_mix_f32 v6, v16, v16, v6 op_sel_hi:[1,1,0]
	ds_read_b128 v[8:11], v22 offset:112
	s_waitcnt lgkmcnt(1)
	v_cvt_f16_f32_e32 v16, v12
	v_cvt_f16_f32_e32 v17, v13
	global_store_dwordx4 v[20:21], v[2:5], off offset:1024
	s_nop 1
	v_cvt_f16_f32_e32 v2, v14
	v_cvt_f16_f32_e32 v4, v15
	v_fma_mix_f32 v3, v16, v16, v6 op_sel_hi:[1,1,0]
	s_nop 0
	v_fma_mix_f32 v3, v17, v17, v3 op_sel_hi:[1,1,0]
	s_nop 0
	v_fma_mix_f32 v5, v2, v2, v3 op_sel_hi:[1,1,0]
	v_cvt_pk_f16_f32 v2, v12, v13
	v_fma_mix_f32 v6, v4, v4, v5 op_sel_hi:[1,1,0]
	s_waitcnt lgkmcnt(0)
	v_cvt_pk_f16_f32 v4, v8, v9
	v_cvt_f32_f16_e32 v8, v4
	v_cvt_f32_f16_sdwa v9, v4 dst_sel:DWORD dst_unused:UNUSED_PAD src0_sel:WORD_1
	v_cvt_pk_f16_f32 v5, v10, v11
	v_cvt_f32_f16_e32 v10, v5
	v_cvt_f32_f16_sdwa v11, v5 dst_sel:DWORD dst_unused:UNUSED_PAD src0_sel:WORD_1
	v_pk_mul_f32 v[8:9], v[8:9], v[8:9]
	v_cvt_pk_f16_f32 v3, v14, v15
	v_add_f32_e32 v6, v6, v8
	v_add_f32_e32 v6, v6, v9
	v_pk_mul_f32 v[12:13], v[10:11], v[10:11]
	ds_read_b128 v[8:11], v22 offset:128
	global_store_dwordx4 v[20:21], v[2:5], off offset:1536
	ds_read_b128 v[2:5], v22 offset:144
	v_add_f32_e32 v6, v6, v12
	v_add_f32_e32 v6, v6, v13
	s_waitcnt lgkmcnt(1)
	v_cvt_pk_f16_f32 v8, v8, v9
	v_cvt_f32_f16_e32 v12, v8
	v_cvt_f32_f16_sdwa v13, v8 dst_sel:DWORD dst_unused:UNUSED_PAD src0_sel:WORD_1
	v_cvt_pk_f16_f32 v9, v10, v11
	v_cvt_f32_f16_e32 v14, v9
	v_cvt_f32_f16_sdwa v15, v9 dst_sel:DWORD dst_unused:UNUSED_PAD src0_sel:WORD_1
	s_waitcnt lgkmcnt(0)
	v_cvt_pk_f16_f32 v10, v2, v3
	v_cvt_f32_f16_e32 v2, v10
	v_cvt_f32_f16_sdwa v3, v10 dst_sel:DWORD dst_unused:UNUSED_PAD src0_sel:WORD_1
	v_pk_mul_f32 v[12:13], v[12:13], v[12:13]
	v_cvt_pk_f16_f32 v11, v4, v5
	v_add_f32_e32 v6, v6, v12
	v_cvt_f32_f16_e32 v4, v11
	v_cvt_f32_f16_sdwa v5, v11 dst_sel:DWORD dst_unused:UNUSED_PAD src0_sel:WORD_1
	v_pk_mul_f32 v[14:15], v[14:15], v[14:15]
	v_add_f32_e32 v6, v6, v13
	v_add_f32_e32 v6, v6, v14
	v_pk_mul_f32 v[2:3], v[2:3], v[2:3]
	v_add_f32_e32 v6, v6, v15
	v_add_f32_e32 v2, v6, v2
	v_pk_mul_f32 v[4:5], v[4:5], v[4:5]
	v_add_f32_e32 v2, v2, v3
	v_add_f32_e32 v2, v2, v4
	v_add_f32_e32 v2, v2, v5
	v_mul_f32_e32 v3, 0x4f800000, v2
	v_cmp_gt_f32_e32 vcc, s4, v2
	global_store_dwordx4 v[20:21], v[8:11], off offset:2048
	v_mov_b32_e32 v6, 0x3c00
	v_cndmask_b32_e32 v2, v2, v3, vcc
	v_sqrt_f32_e32 v3, v2
	v_mov_b32_e32 v8, v7
	v_mov_b32_e32 v9, v7
	global_store_dwordx4 v[20:21], v[6:9], off offset:2560
	v_add_u32_e32 v4, -1, v3
	v_fma_f32 v5, -v4, v3, v2
	v_cmp_ge_f32_e64 s[4:5], 0, v5
	v_add_u32_e32 v5, 1, v3
	s_nop 0
	v_cndmask_b32_e64 v4, v3, v4, s[4:5]
	v_fma_f32 v3, -v5, v3, v2
	v_cmp_lt_f32_e64 s[4:5], 0, v3
	s_nop 1
	v_cndmask_b32_e64 v3, v4, v5, s[4:5]
	v_mul_f32_e32 v4, 0x37800000, v3
	v_cndmask_b32_e32 v3, v3, v4, vcc
	v_mov_b32_e32 v4, 0x260
	v_cmp_class_f32_e32 vcc, v2, v4
	s_nop 1
	v_cndmask_b32_e32 v2, v3, v2, vcc

.LBB2_131:
	v_cmp_eq_u32_e32 vcc, 0, v0
	s_and_saveexec_b64 s[2:3], vcc
	s_cbranch_execz .LBB2_133
	v_mov_b32_e32 v2, 0x10800
	ds_read_b128 v[2:5], v2
	s_mov_b64 s[4:5], s[50:51]
	s_lshl_b32 s8, s22, 2
	s_waitcnt lgkmcnt(0)
	v_max_f32_e32 v5, v5, v5
	v_max_f32_e32 v4, v4, v4
	v_max_f32_e32 v4, v4, v5
	v_max3_f32 v2, v2, v3, v4
	v_mov_b32_e32 v3, s8
	global_store_dword v3, v2, s[4:5]

.LBB2_137:
	s_andn2_b64 vcc, exec, s[2:3]
	s_cbranch_vccnz .LBB2_140
	s_andn2_b64 vcc, exec, s[10:11]
	s_cbranch_vccnz .LBB2_140
	v_and_b32_e32 v3, 3, v0
	v_lshrrev_b32_e32 v2, 2, v0
	v_mul_u32_u24_e32 v3, 0xa0, v3
	s_movk_i32 s2, 0x310
	v_mad_u32_u24 v5, v2, s2, v3
	ds_read_b96 v[8:10], v5
	v_mov_b32_e32 v2, 0x3e21e89b
	v_mul_f32_e32 v2, s23, v2
	v_mul_f32_e32 v4, 0x3fb8aa3b, v2
	ds_read2_b32 v[2:3], v5 offset0:3 offset1:4
	s_waitcnt lgkmcnt(1)
	v_mov_b32_e32 v6, v9
	v_mov_b32_e32 v7, v10
	v_pk_mul_f32 v[6:7], v[4:5], v[6:7] op_sel_hi:[0,1]
	v_cvt_pk_f16_f32 v7, v6, v7
	v_cvt_f32_f16_e32 v9, v7
	s_waitcnt lgkmcnt(0)
	v_pk_mul_f32 v[2:3], v[4:5], v[2:3] op_sel_hi:[0,1]
	v_cvt_pk_f16_f32 v10, v2, v3
	ds_read2_b32 v[2:3], v5 offset0:5 offset1:6
	v_fma_mixlo_f16 v8, v4, v8, 0
	v_mul_f32_e32 v9, v9, v9
	v_fma_mix_f32 v9, v8, v8, v9 op_sel_hi:[1,1,0]
	ds_read2_b32 v[12:13], v5 offset0:7 offset1:8
	ds_read2_b32 v[14:15], v5 offset0:9 offset1:10
	ds_read2_b32 v[16:17], v5 offset0:11 offset1:12
	v_fma_mix_f32 v9, v7, v7, v9 op_sel:[1,1,0] op_sel_hi:[1,1,0]
	s_waitcnt lgkmcnt(3)
	v_pk_mul_f32 v[2:3], v[4:5], v[2:3] op_sel_hi:[0,1]
	v_fma_mix_f32 v11, v10, v10, v9 op_sel_hi:[1,1,0]
	s_mov_b64 s[4:5], s[44:45]
	s_mov_b64 s[6:7], s[46:47]
	v_pack_b32_f16 v8, v8, v7
	v_alignbit_b32 v9, v10, v7, 16
	v_fma_mix_f32 v7, v10, v10, v11 op_sel:[1,1,0] op_sel_hi:[1,1,0]
	v_cvt_pk_f16_f32 v2, v2, v3
	v_lshl_add_u32 v6, s22, 8, v0
	v_fma_mix_f32 v3, v2, v2, v7 op_sel_hi:[1,1,0]
	v_lshrrev_b32_e32 v18, 5, v6
	v_alignbit_b32 v10, v2, v10, 16
	v_lshrrev_b32_e32 v11, 16, v2
	v_fma_mix_f32 v2, v2, v2, v3 op_sel:[1,1,0] op_sel_hi:[1,1,0]
	s_waitcnt lgkmcnt(0)
	v_fma_mixlo_f16 v3, v4, v12, 0
	s_movk_i32 s2, 0xc0
	v_fma_mix_f32 v7, v3, v3, v2 op_sel_hi:[1,1,0]
	v_mul_lo_u32 v2, v18, s2
	v_and_or_b32 v2, v0, 31, v2
	v_mov_b32_e32 v3, 0
	v_fma_mixhi_f16 v11, v4, v12, 0
	v_lshl_add_u64 v[18:19], v[2:3], 4, s[4:5]
	global_store_dwordx4 v[18:19], v[8:11], off
	s_mov_b32 s2, 0xf800000
	s_nop 0
	v_pk_mul_f32 v[8:9], v[4:5], v[14:15] op_sel_hi:[0,1]
	v_fma_mixlo_f16 v10, v4, v13, 0
	v_cvt_pk_f16_f32 v9, v8, v9
	v_fma_mix_f32 v7, v10, v10, v7 op_sel_hi:[1,1,0]
	v_pack_b32_f16 v8, v10, v9
	v_pk_mul_f32 v[10:11], v[4:5], v[16:17] op_sel_hi:[0,1]
	v_cvt_pk_f16_f32 v18, v10, v11
	ds_read2_b32 v[10:11], v5 offset0:13 offset1:14
	v_fma_mix_f32 v7, v9, v9, v7 op_sel_hi:[1,1,0]
	ds_read2_b32 v[12:13], v5 offset0:15 offset1:16
	ds_read2_b32 v[14:15], v5 offset0:17 offset1:18
	ds_read2_b32 v[16:17], v5 offset0:19 offset1:20
	v_fma_mix_f32 v7, v9, v9, v7 op_sel:[1,1,0] op_sel_hi:[1,1,0]
	v_alignbit_b32 v9, v18, v9, 16
	v_fma_mix_f32 v7, v18, v18, v7 op_sel_hi:[1,1,0]
	s_waitcnt lgkmcnt(3)
	v_pk_mul_f32 v[10:11], v[4:5], v[10:11] op_sel_hi:[0,1]
	v_fma_mix_f32 v7, v18, v18, v7 op_sel:[1,1,0] op_sel_hi:[1,1,0]
	v_cvt_pk_f16_f32 v19, v10, v11
	v_fma_mix_f32 v7, v19, v19, v7 op_sel_hi:[1,1,0]
	v_alignbit_b32 v10, v19, v18, 16
	v_fma_mix_f32 v7, v19, v19, v7 op_sel:[1,1,0] op_sel_hi:[1,1,0]
	s_waitcnt lgkmcnt(2)
	v_fma_mixlo_f16 v18, v4, v12, 0
	v_lshrrev_b32_e32 v11, 16, v19
	v_fma_mix_f32 v7, v18, v18, v7 op_sel_hi:[1,1,0]
	v_ashrrev_i32_e32 v19, 31, v2
	v_mov_b32_e32 v18, v2
	v_fma_mixhi_f16 v11, v4, v12, 0
	v_lshl_add_u64 v[18:19], v[18:19], 4, s[4:5]
	global_store_dwordx4 v[18:19], v[8:11], off offset:512
	s_waitcnt lgkmcnt(1)
	s_nop 0
	v_pk_mul_f32 v[8:9], v[4:5], v[14:15] op_sel_hi:[0,1]
	v_fma_mixlo_f16 v10, v4, v13, 0
	v_cvt_pk_f16_f32 v9, v8, v9
	v_fma_mix_f32 v7, v10, v10, v7 op_sel_hi:[1,1,0]
	v_pack_b32_f16 v8, v10, v9
	s_waitcnt lgkmcnt(0)
	v_pk_mul_f32 v[10:11], v[4:5], v[16:17] op_sel_hi:[0,1]
	v_cvt_pk_f16_f32 v18, v10, v11
	ds_read2_b32 v[10:11], v5 offset0:21 offset1:22
	v_fma_mix_f32 v7, v9, v9, v7 op_sel_hi:[1,1,0]
	ds_read2_b32 v[12:13], v5 offset0:23 offset1:24
	ds_read2_b32 v[14:15], v5 offset0:25 offset1:26
	ds_read2_b32 v[16:17], v5 offset0:27 offset1:28
	v_fma_mix_f32 v7, v9, v9, v7 op_sel:[1,1,0] op_sel_hi:[1,1,0]
	v_alignbit_b32 v9, v18, v9, 16
	v_fma_mix_f32 v7, v18, v18, v7 op_sel_hi:[1,1,0]
	s_waitcnt lgkmcnt(3)
	v_pk_mul_f32 v[10:11], v[4:5], v[10:11] op_sel_hi:[0,1]
	v_fma_mix_f32 v7, v18, v18, v7 op_sel:[1,1,0] op_sel_hi:[1,1,0]
	v_cvt_pk_f16_f32 v19, v10, v11
	v_fma_mix_f32 v7, v19, v19, v7 op_sel_hi:[1,1,0]
	v_alignbit_b32 v10, v19, v18, 16
	v_fma_mix_f32 v7, v19, v19, v7 op_sel:[1,1,0] op_sel_hi:[1,1,0]
	s_waitcnt lgkmcnt(2)
	v_fma_mixlo_f16 v18, v4, v12, 0
	v_lshrrev_b32_e32 v11, 16, v19
	v_fma_mix_f32 v7, v18, v18, v7 op_sel_hi:[1,1,0]
	v_add_u32_e32 v18, 64, v2
	v_mov_b32_e32 v19, v3
	v_fma_mixhi_f16 v11, v4, v12, 0
	v_lshl_add_u64 v[20:21], v[18:19], 4, s[4:5]
	global_store_dwordx4 v[20:21], v[8:11], off
	s_waitcnt lgkmcnt(1)
	s_nop 0
	v_pk_mul_f32 v[8:9], v[4:5], v[14:15] op_sel_hi:[0,1]
	v_fma_mixlo_f16 v10, v4, v13, 0
	v_cvt_pk_f16_f32 v9, v8, v9
	v_fma_mix_f32 v7, v10, v10, v7 op_sel_hi:[1,1,0]
	v_pack_b32_f16 v8, v10, v9
	s_waitcnt lgkmcnt(0)
	v_pk_mul_f32 v[10:11], v[4:5], v[16:17] op_sel_hi:[0,1]
	v_cvt_pk_f16_f32 v19, v10, v11
	ds_read2_b32 v[10:11], v5 offset0:29 offset1:30
	ds_read2_b32 v[12:13], v5 offset0:31 offset1:32
	ds_read2_b32 v[14:15], v5 offset0:33 offset1:34
	ds_read2_b32 v[16:17], v5 offset0:35 offset1:36
	v_fma_mix_f32 v7, v9, v9, v7 op_sel_hi:[1,1,0]
	s_waitcnt lgkmcnt(2)
	v_fma_mixlo_f16 v21, v4, v12, 0
	v_pk_mul_f32 v[10:11], v[4:5], v[10:11] op_sel_hi:[0,1]
	v_cvt_pk_f16_f32 v10, v10, v11
	v_fma_mix_f32 v7, v9, v9, v7 op_sel:[1,1,0] op_sel_hi:[1,1,0]
	v_lshrrev_b32_e32 v11, 16, v10
	v_fma_mix_f32 v7, v19, v19, v7 op_sel_hi:[1,1,0]
	v_cvt_f32_f16_e32 v20, v11
	v_cvt_f32_f16_e32 v21, v21
	v_fma_mix_f32 v7, v19, v19, v7 op_sel:[1,1,0] op_sel_hi:[1,1,0]
	v_alignbit_b32 v9, v19, v9, 16
	v_fma_mix_f32 v7, v10, v10, v7 op_sel_hi:[1,1,0]
	v_alignbit_b32 v10, v10, v19, 16
	v_ashrrev_i32_e32 v19, 31, v18
	v_fma_mixhi_f16 v11, v4, v12, 0
	v_lshl_add_u64 v[18:19], v[18:19], 4, s[4:5]
	v_pk_mul_f32 v[20:21], v[20:21], v[20:21]
	s_waitcnt lgkmcnt(1)
	v_pk_mul_f32 v[14:15], v[4:5], v[14:15] op_sel_hi:[0,1]
	global_store_dwordx4 v[18:19], v[8:11], off offset:512
	v_add_f32_e32 v7, v7, v20
	v_cvt_pk_f16_f32 v20, v14, v15
	s_waitcnt lgkmcnt(0)
	v_pk_mul_f32 v[10:11], v[4:5], v[16:17] op_sel_hi:[0,1]
	v_cvt_pk_f16_f32 v19, v10, v11
	ds_read2_b32 v[10:11], v5 offset0:37 offset1:38
	ds_read_b32 v5, v5 offset:156
	v_cvt_f32_f16_e32 v14, v20
	v_cvt_f32_f16_sdwa v15, v20 dst_sel:DWORD dst_unused:UNUSED_PAD src0_sel:WORD_1
	v_fma_mixlo_f16 v18, v4, v13, 0
	v_add_f32_e32 v7, v7, v21
	s_waitcnt lgkmcnt(0)
	v_pk_mul_f32 v[10:11], v[4:5], v[10:11] op_sel_hi:[0,1]
	v_pk_mul_f32 v[12:13], v[14:15], v[14:15]
	v_cvt_f32_f16_e32 v14, v19
	v_cvt_f32_f16_sdwa v15, v19 dst_sel:DWORD dst_unused:UNUSED_PAD src0_sel:WORD_1
	v_pack_b32_f16 v8, v18, v20
	v_alignbit_b32 v9, v19, v20, 16
	v_cvt_pk_f16_f32 v20, v10, v11
	v_fma_mixlo_f16 v10, v4, v5, 0
	v_lshrrev_b32_e32 v11, 16, v20
	v_fma_mix_f32 v7, v18, v18, v7 op_sel_hi:[1,1,0]
	v_cvt_f32_f16_e32 v16, v11
	v_cvt_f32_f16_e32 v17, v10
	v_add_f32_e32 v7, v7, v12
	v_pk_mul_f32 v[14:15], v[14:15], v[14:15]
	v_add_f32_e32 v7, v7, v13
	v_add_f32_e32 v7, v7, v14
	v_add_f32_e32 v7, v7, v15
	v_fma_mixhi_f16 v11, v4, v5, 0
	v_pk_mul_f32 v[4:5], v[16:17], v[16:17]
	v_fma_mix_f32 v7, v20, v20, v7 op_sel_hi:[1,1,0]
	v_add_u32_e32 v16, 0x80, v2
	v_add_f32_e32 v4, v7, v4
	v_add_f32_e32 v4, v4, v5
	v_mov_b32_e32 v17, v3
	v_mul_f32_e32 v5, 0x4f800000, v4
	v_cmp_gt_f32_e32 vcc, s2, v4
	v_alignbit_b32 v10, v20, v19, 16
	v_lshl_add_u64 v[16:17], v[16:17], 4, s[4:5]
	v_cndmask_b32_e32 v7, v4, v5, vcc
	global_store_dwordx4 v[16:17], v[8:11], off
	v_add_u32_e32 v2, 0xa0, v2
	v_mov_b32_e32 v4, v3
	v_sqrt_f32_e32 v10, v7
	v_lshl_add_u64 v[8:9], v[2:3], 4, s[4:5]
	v_mov_b32_e32 v2, v3
	v_mov_b32_e32 v5, v3
	global_store_dwordx4 v[8:9], v[2:5], off
	s_nop 1
	v_add_u32_e32 v2, -1, v10
	v_fma_f32 v4, -v2, v10, v7
	v_cmp_ge_f32_e64 s[2:3], 0, v4
	v_add_u32_e32 v4, 1, v10
	v_fma_f32 v5, -v4, v10, v7
	v_cndmask_b32_e64 v2, v10, v2, s[2:3]
	v_cmp_lt_f32_e64 s[2:3], 0, v5
	s_nop 1
	v_cndmask_b32_e64 v2, v2, v4, s[2:3]
	v_mul_f32_e32 v4, 0x37800000, v2
	v_cndmask_b32_e32 v2, v2, v4, vcc
	v_mov_b32_e32 v4, 0x260
	v_cmp_class_f32_e32 vcc, v7, v4
	s_nop 1
	v_cndmask_b32_e32 v4, v2, v7, vcc
	v_mov_b32_e32 v7, v3
	v_lshl_add_u64 v[2:3], v[6:7], 2, s[6:7]
	global_store_dword v[2:3], v4, off

.LBB2_141:
	s_and_b64 vcc, exec, s[2:3]
	s_cbranch_vccz .LBB2_148
	s_mov_b64 s[0:1], s[42:43]
	s_andn2_b64 vcc, exec, s[10:11]
	s_cbranch_vccnz .LBB2_144
	s_and_b32 s2, s21, 0xc0
	s_lshl_b32 s2, s2, 1
	v_lshl_or_b32 v1, v1, 4, s2
	s_movk_i32 s2, 0x210
	v_mad_u32_u24 v1, v147, s2, v1
	ds_read_b128 v[2:5], v1
	ds_read_b128 v[6:9], v1 offset:16896
	ds_read_b128 v[10:13], v1 offset:64
	ds_read_b128 v[14:17], v1 offset:16960
	ds_read_b128 v[22:25], v1 offset:25344
	ds_read_b128 v[26:29], v1 offset:25408
	ds_read_b128 v[34:37], v1 offset:33792
	ds_read_b128 v[38:41], v1 offset:33856
	ds_read_b128 v[42:45], v1 offset:8448
	ds_read_b128 v[46:49], v1 offset:8512
	s_waitcnt lgkmcnt(0)
	v_mfma_f32_16x16x32_f16 v[18:21], v[2:5], v[6:9], 0
	s_mulk_i32 s20, 0x1800
	v_lshl_or_b32 v1, v146, 2, s20
	v_mfma_f32_16x16x32_f16 v[30:33], v[2:5], v[22:25], 0
	v_mfma_f32_16x16x32_f16 v[2:5], v[2:5], v[34:37], 0
	v_mfma_f32_16x16x32_f16 v[6:9], v[42:45], v[6:9], 0
	v_mfma_f32_16x16x32_f16 v[22:25], v[42:45], v[22:25], 0
	v_mfma_f32_16x16x32_f16 v[18:21], v[10:13], v[14:17], v[18:21]
	v_mfma_f32_16x16x32_f16 v[2:5], v[10:13], v[38:41], v[2:5]
	v_mfma_f32_16x16x32_f16 v[30:33], v[10:13], v[26:29], v[30:33]
	s_nop 5
	ds_write2st64_b32 v1, v18, v19 offset0:165 offset1:166
	ds_write2st64_b32 v1, v20, v21 offset0:167 offset1:168
	ds_write2st64_b32 v1, v30, v31 offset0:169 offset1:170
	ds_write2st64_b32 v1, v32, v33 offset0:171 offset1:172
	v_mfma_f32_16x16x32_f16 v[6:9], v[46:49], v[14:17], v[6:9]
	ds_write2st64_b32 v1, v2, v3 offset0:173 offset1:174
	ds_write2st64_b32 v1, v4, v5 offset0:175 offset1:176
	s_nop 5
	ds_write2st64_b32 v1, v6, v7 offset0:177 offset1:178
	v_mfma_f32_16x16x32_f16 v[34:37], v[42:45], v[34:37], 0
	v_mfma_f32_16x16x32_f16 v[2:5], v[46:49], v[26:29], v[22:25]
	ds_write2st64_b32 v1, v8, v9 offset0:179 offset1:180
	s_nop 6
	ds_write2st64_b32 v1, v2, v3 offset0:181 offset1:182
	ds_write2st64_b32 v1, v4, v5 offset0:183 offset1:184
	v_mfma_f32_16x16x32_f16 v[2:5], v[46:49], v[38:41], v[34:37]
	s_nop 7
	ds_write2st64_b32 v1, v2, v3 offset0:185 offset1:186
	ds_write2st64_b32 v1, v4, v5 offset0:187 offset1:188

_Z8k_embed2PKfS0_S0_S0_S0_S0_S0_S0_S0_S0_PDF16_S0_S0_S0_S0_S0_S0_PDv8_DF16_:
	s_load_dwordx16 s[36:51], s[0:1], 0x0
	s_load_dwordx16 s[52:67], s[0:1], 0x40
	s_load_dwordx4 s[68:71], s[0:1], 0x80
	v_readfirstlane_b32 s30, v0
	s_cmpk_gt_i32 s2, 0xff
	s_mov_b64 s[4:5], -1
	s_waitcnt lgkmcnt(0)
	s_cbranch_scc0 .LBB5_196
	v_lshl_or_b32 v1, s2, 9, v0
	v_add_u32_e32 v2, 0xfffe0000, v1
	s_movk_i32 s3, 0x3e80
	v_cmp_gt_i32_e32 vcc, s3, v2
	s_and_saveexec_b64 s[14:15], vcc
	s_cbranch_execz .LBB5_195
	v_lshrrev_b32_e32 v1, 6, v2
	s_mov_b32 s3, 0x33333334
	v_mul_hi_u32 v3, v1, s3
	v_mul_u32_u24_e32 v3, 5, v3
	s_mov_b32 s3, 0xcccccccd
	v_sub_u32_e32 v3, v1, v3
	v_mul_hi_u32 v1, v2, s3
	v_lshrrev_b32_e32 v1, 4, v1
	v_and_b32_e32 v4, 15, v0
	s_mov_b32 s3, 0xffffff0
	v_and_or_b32 v1, v1, s3, v4
	s_movk_i32 s3, 0x9ff
	v_cmp_lt_u32_e64 s[10:11], s3, v2
	s_movk_i32 s3, 0x167f
	v_cmp_lt_u32_e64 s[8:9], s3, v2
	s_movk_i32 s3, 0x22ff
	s_mov_b64 s[24:25], s[66:67]
	s_mov_b64 s[26:27], s[68:69]
	s_mov_b64 s[16:17], s[58:59]
	s_mov_b64 s[18:19], s[60:61]
	s_mov_b64 s[20:21], s[62:63]
	s_mov_b64 s[22:23], s[64:65]
	v_cmp_lt_u32_e64 s[6:7], s3, v2
	s_movk_i32 s3, 0x2f7f
	v_cmp_lt_u32_e64 s[4:5], s3, v2
	s_movk_i32 s3, 0x31ff
	v_cmp_lt_u32_e64 s[12:13], s3, v2
	s_movk_i32 s3, 0xa0
	v_mov_b32_e32 v17, 0
	v_mul_lo_u32 v10, v1, s3
	v_mov_b32_e32 v11, v17
	v_lshlrev_b64 v[14:15], 2, v[10:11]
	v_add_u32_e32 v6, 0xfffe7000, v10
	s_waitcnt lgkmcnt(0)
	v_lshl_add_u64 v[12:13], s[18:19], 0, v[14:15]
	s_mov_b32 s18, 0xfffd3000
	v_ashrrev_i32_e32 v7, 31, v6
	s_mov_b32 s19, -1
	v_lshrrev_b32_e32 v4, 1, v0
	v_lshl_add_u64 v[8:9], v[6:7], 2, s[22:23]
	s_mov_b32 s22, 0xfffba000
	v_lshl_add_u64 v[12:13], v[12:13], 0, s[18:19]
	s_mov_b32 s18, 0xfffec000
	v_and_b32_e32 v4, 24, v4
	v_lshlrev_b32_e32 v16, 5, v1
	v_lshl_add_u64 v[10:11], s[24:25], 0, v[14:15]
	s_mov_b32 s23, -1
	v_lshl_add_u64 v[14:15], s[20:21], 0, v[14:15]
	s_mov_b32 s19, -1
	v_lshl_or_b32 v4, v3, 5, v4
	v_lshl_add_u64 v[6:7], v[16:17], 2, s[26:27]
	v_lshl_add_u64 v[10:11], v[10:11], 0, s[22:23]
	v_lshl_add_u64 v[14:15], v[14:15], 0, s[18:19]
	v_lshlrev_b32_e32 v16, 7, v1
	s_and_saveexec_b64 s[18:19], s[10:11]
	s_xor_b64 s[18:19], exec, s[18:19]
	s_cbranch_execz .LBB5_142
	s_and_saveexec_b64 s[20:21], s[8:9]
	s_xor_b64 s[20:21], exec, s[20:21]
	s_cbranch_execz .LBB5_19
	s_and_saveexec_b64 s[22:23], s[6:7]
	s_xor_b64 s[22:23], exec, s[22:23]
	s_cbranch_execz .LBB5_16
	s_and_saveexec_b64 s[24:25], s[4:5]
	s_xor_b64 s[24:25], exec, s[24:25]
	s_cbranch_execz .LBB5_13
	s_and_saveexec_b64 s[26:27], s[12:13]
	s_xor_b64 s[26:27], exec, s[26:27]
	s_cbranch_execz .LBB5_8
	v_mov_b32_e32 v5, 0
	v_lshl_add_u64 v[18:19], v[4:5], 2, v[8:9]
	global_load_dword v1, v[18:19], off nt

.LBB5_170:
	s_or_b64 exec, exec, s[16:17]
	s_mov_b64 s[16:17], s[70:71]
	s_and_saveexec_b64 s[18:19], s[10:11]
	s_xor_b64 s[10:11], exec, s[18:19]
	s_cbranch_execz .LBB5_190
	v_or_b32_e32 v16, 7, v4
	s_and_saveexec_b64 s[18:19], s[8:9]
	s_xor_b64 s[8:9], exec, s[18:19]
	s_cbranch_execz .LBB5_187
	s_and_saveexec_b64 s[18:19], s[6:7]
	s_xor_b64 s[6:7], exec, s[18:19]
	s_cbranch_execz .LBB5_184
	s_and_saveexec_b64 s[18:19], s[4:5]
	s_xor_b64 s[4:5], exec, s[18:19]
	s_cbranch_execz .LBB5_181
	s_and_saveexec_b64 s[18:19], s[12:13]
	s_xor_b64 s[12:13], exec, s[18:19]
	s_cbranch_execz .LBB5_176
	v_mov_b32_e32 v5, 0
	v_lshl_add_u64 v[4:5], v[4:5], 2, v[8:9]
	global_load_dword v5, v[4:5], off offset:28 nt

.LBB5_196:
	s_andn2_b64 vcc, exec, s[4:5]
	s_cbranch_vccnz .LBB5_225
	s_movk_i32 s3, 0xe0
	v_cmp_gt_u32_e32 vcc, s3, v0
	s_movk_i32 s3, 0xdf
	v_cmp_lt_u32_e64 s[4:5], s3, v0
	v_lshlrev_b32_e32 v76, 2, v0
	s_and_saveexec_b64 s[6:7], s[4:5]
	s_xor_b64 s[4:5], exec, s[6:7]
	v_lshlrev_b32_e32 v76, 2, v0
	s_or_saveexec_b64 s[8:9], s[4:5]
	s_mov_b64 s[4:5], s[46:47]
	s_mov_b64 s[6:7], s[48:49]
	s_mov_b64 s[10:11], s[50:51]
	s_ashr_i32 s15, s2, 4
	s_and_b32 s14, s2, 15
	v_mov_b32_e32 v58, 0
	v_lshlrev_b32_e32 v1, 6, v0
	v_mov_b32_e32 v62, 0
	v_mov_b32_e32 v63, 0
	v_mov_b32_e32 v64, 0
	v_mov_b32_e32 v65, 0
	s_xor_b64 exec, exec, s[8:9]
	s_cbranch_execz .LBB5_201
	s_mov_b64 s[2:3], s[38:39]
	v_lshlrev_b32_e32 v2, 12, v0
	v_and_b32_e32 v6, 0x400, v1
	v_mov_b32_e32 v3, 0
	v_and_b32_e32 v2, 0xe0000, v2
	v_lshl_or_b32 v6, s15, 11, v6
	s_waitcnt lgkmcnt(0)
	v_lshl_add_u64 v[4:5], s[2:3], 0, v[2:3]
	v_ashrrev_i32_e32 v7, 31, v6
	v_lshl_add_u64 v[4:5], v[6:7], 2, v[4:5]
	v_lshlrev_b32_e32 v6, 4, v0
	v_and_b32_e32 v2, 0x80, v6
	v_lshl_or_b32 v2, s14, 8, v2
	v_lshl_add_u64 v[4:5], v[4:5], 0, v[2:3]
	v_and_b32_e32 v2, 0x70, v6
	v_lshl_add_u64 v[2:3], v[4:5], 0, v[2:3]
	global_load_dwordx4 v[62:65], v[2:3], off nt
.LBB5_201:
	s_or_b64 exec, exec, s[8:9]
	s_mov_b64 s[2:3], s[36:37]
	s_mov_b64 s[12:13], s[40:41]
	s_cmpk_lt_u32 s30, 0x1c0
	s_cselect_b64 s[8:9], -1, 0
	s_cmpk_gt_u32 s30, 0x1bf
	v_mov_b32_e32 v59, 0
	v_mov_b32_e32 v60, 0
	v_mov_b32_e32 v61, 0
	s_cbranch_scc1 .LBB5_203
	s_mov_b64 s[16:17], s[44:45]
	v_mov_b32_e32 v77, 0
	s_waitcnt lgkmcnt(0)
	v_lshl_add_u64 v[2:3], v[76:77], 2, s[16:17]
	global_load_dwordx4 v[58:61], v[2:3], off
.LBB5_203:
	v_lshrrev_b32_e32 v81, 4, v0
	v_lshlrev_b32_e32 v79, 2, v81
	s_waitcnt lgkmcnt(0)
	global_load_dword v80, v79, s[4:5]
	s_lshr_b32 s4, s30, 2
	s_and_b32 s4, s4, 0x3ffffff0
	v_lshrrev_b32_e32 v77, 5, v0
	v_and_or_b32 v66, v77, 1, s4
	v_mov_b32_e32 v67, 0
	v_and_b32_e32 v1, 0x400, v1
	v_lshlrev_b64 v[2:3], 17, v[66:67]
	v_lshl_or_b32 v4, s15, 11, v1
	v_and_b32_e32 v1, 32, v76
	v_lshl_add_u64 v[2:3], s[2:3], 0, v[2:3]
	v_ashrrev_i32_e32 v5, 31, v4
	v_lshlrev_b32_e32 v1, 2, v1
	v_and_b32_e32 v78, 7, v0
	v_lshl_add_u64 v[2:3], v[4:5], 2, v[2:3]
	v_lshl_or_b32 v4, s14, 8, v1
	v_mov_b32_e32 v5, v67
	v_lshl_add_u64 v[2:3], v[2:3], 0, v[4:5]
	v_lshlrev_b32_e32 v4, 4, v78
	v_lshl_add_u64 v[2:3], v[2:3], 0, v[4:5]
	s_mov_b32 s2, 0x40000
	v_add_co_u32_e64 v4, s[2:3], s2, v2
	s_lshl_b32 s16, s15, 8
	s_nop 0
	v_addc_co_u32_e64 v5, s[2:3], 0, v3, s[2:3]
	s_mov_b32 s2, 0x80000
	global_load_dwordx4 v[54:57], v[2:3], off nt
	global_load_dwordx4 v[50:53], v[4:5], off nt
	v_add_co_u32_e64 v4, s[2:3], s2, v2
	s_lshl_b32 s17, s14, 4
	s_nop 0
	v_addc_co_u32_e64 v5, s[2:3], 0, v3, s[2:3]
	s_mov_b32 s2, 0xc0000
	s_nop 0
	v_add_co_u32_e64 v6, s[2:3], s2, v2
	s_or_b32 s16, s16, s17
	s_nop 0
	v_addc_co_u32_e64 v7, s[2:3], 0, v3, s[2:3]
	s_mov_b32 s2, 0x100000
	global_load_dwordx4 v[46:49], v[4:5], off nt
	global_load_dwordx4 v[42:45], v[6:7], off nt
	v_add_co_u32_e64 v4, s[2:3], s2, v2
	v_or_b32_e32 v70, s16, v77
	s_nop 0
	v_addc_co_u32_e64 v5, s[2:3], 0, v3, s[2:3]
	s_mov_b32 s2, 0x140000
	s_nop 0
	v_add_co_u32_e64 v6, s[2:3], s2, v2
	v_ashrrev_i32_e32 v71, 31, v70
	s_nop 0
	v_addc_co_u32_e64 v7, s[2:3], 0, v3, s[2:3]
	s_mov_b32 s2, 0x180000
	global_load_dwordx4 v[34:37], v[4:5], off nt
	global_load_dwordx4 v[26:29], v[6:7], off nt
	v_add_co_u32_e64 v4, s[2:3], s2, v2
	v_lshlrev_b64 v[6:7], 9, v[70:71]
	s_nop 0
	v_addc_co_u32_e64 v5, s[2:3], 0, v3, s[2:3]
	s_mov_b32 s2, 0x1c0000
	v_and_b32_e32 v1, 0x7c, v76
	v_add_co_u32_e64 v2, s[2:3], s2, v2
	v_lshl_add_u64 v[6:7], s[12:13], 0, v[6:7]
	v_lshlrev_b32_e32 v74, 2, v1
	v_mov_b32_e32 v75, v67
	v_addc_co_u32_e64 v3, s[2:3], 0, v3, s[2:3]
	v_lshl_add_u64 v[6:7], v[6:7], 0, v[74:75]
	global_load_dwordx4 v[38:41], v[4:5], off nt
	global_load_dwordx4 v[30:33], v[2:3], off nt
	global_load_dwordx4 v[22:25], v[6:7], off nt
	global_load_dwordx4 v[10:13], v74, s[6:7]
	global_load_dwordx4 v[14:17], v74, s[10:11]
	v_lshlrev_b32_e32 v71, 2, v78
	v_bfe_u32 v75, v0, 3, 4
	s_cmpk_lt_u32 s30, 0x80
	s_cselect_b64 s[2:3], -1, 0
	s_cmpk_gt_u32 s30, 0x7f
	v_mov_b32_e32 v7, v67
	v_mov_b32_e32 v2, v67
	v_mov_b32_e32 v3, v67
	v_mov_b32_e32 v18, v67
	v_mov_b32_e32 v19, v67
	v_mov_b32_e32 v8, v67
	v_mov_b32_e32 v9, v67
	v_mov_b32_e32 v4, v67
	v_mov_b32_e32 v5, v67
	v_mov_b32_e32 v20, v67
	v_mov_b32_e32 v21, v67
	v_or_b32_e32 v68, s16, v75
	v_lshlrev_b32_e32 v72, 2, v71
	s_cbranch_scc1 .LBB5_226
	s_mov_b64 s[10:11], s[42:43]
	s_mov_b64 s[4:5], s[52:53]
	s_mov_b64 s[6:7], s[54:55]
	v_ashrrev_i32_e32 v69, 31, v68
	v_lshlrev_b64 v[2:3], 7, v[68:69]
	v_mov_b32_e32 v73, 0
	s_waitcnt lgkmcnt(0)
	v_lshl_add_u64 v[2:3], s[10:11], 0, v[2:3]
	v_lshl_add_u64 v[82:83], v[2:3], 0, v[72:73]
	global_load_dwordx4 v[2:5], v72, s[4:5]
	global_load_dwordx4 v[6:9], v72, s[6:7]
	global_load_dwordx4 v[18:21], v[82:83], off nt
	s_waitcnt vmcnt(1)
	v_mov_b32_e32 v67, v6
	v_lshlrev_b32_e32 v6, 2, v76
	s_and_saveexec_b64 s[4:5], vcc
	s_cbranch_execnz .LBB5_227

.LBB5_219:
	s_or_b64 exec, exec, s[4:5]
	s_waitcnt vmcnt(4)
	v_add_f32_e32 v26, v38, v39
	v_add_f32_e32 v27, v40, v41
	s_waitcnt lgkmcnt(1)
	ds_bpermute_b32 v28, v6, v26
	s_waitcnt lgkmcnt(1)
	ds_bpermute_b32 v29, v6, v27
	s_mov_b64 s[4:5], s[56:57]
	s_waitcnt lgkmcnt(0)
	v_add_f32_e32 v26, v26, v28
	v_add_f32_e32 v27, v27, v29
	ds_bpermute_b32 v28, v0, v26
	ds_bpermute_b32 v29, v0, v27
	s_and_saveexec_b64 s[0:1], vcc
	s_cbranch_execz .LBB5_221
	s_waitcnt lgkmcnt(0)
	v_add_f32_e32 v27, v27, v29
	v_add_f32_e32 v26, v26, v28
	v_mul_f32_e32 v26, 0x3e000000, v26
	v_mul_f32_e32 v27, 0x3e000000, v27
	ds_write2_b32 v54, v26, v27 offset0:12 offset1:176

	.amdhsa_kernel _Z8k_embed2PKfS0_S0_S0_S0_S0_S0_S0_S0_S0_PDF16_S0_S0_S0_S0_S0_S0_PDv8_DF16_
		.amdhsa_group_segment_fixed_size 21248
		.amdhsa_private_segment_fixed_size 0
		.amdhsa_kernarg_size 144
		.amdhsa_user_sgpr_count 2
		.amdhsa_user_sgpr_dispatch_ptr 0
		.amdhsa_user_sgpr_queue_ptr 0
		.amdhsa_user_sgpr_kernarg_segment_ptr 1
		.amdhsa_user_sgpr_dispatch_id 0
		.amdhsa_user_sgpr_kernarg_preload_length 0
		.amdhsa_user_sgpr_kernarg_preload_offset 0
		.amdhsa_user_sgpr_private_segment_size 0
		.amdhsa_uses_dynamic_stack 0
		.amdhsa_enable_private_segment 0
		.amdhsa_system_sgpr_workgroup_id_x 1
		.amdhsa_system_sgpr_workgroup_id_y 0
		.amdhsa_system_sgpr_workgroup_id_z 0
		.amdhsa_system_sgpr_workgroup_info 0
		.amdhsa_system_vgpr_workitem_id 0
		.amdhsa_next_free_vgpr 99
		.amdhsa_next_free_sgpr 72
		.amdhsa_accum_offset 100
		.amdhsa_reserve_vcc 1
		.amdhsa_float_round_mode_32 0
		.amdhsa_float_round_mode_16_64 0
		.amdhsa_float_denorm_mode_32 3
		.amdhsa_float_denorm_mode_16_64 3
		.amdhsa_dx10_clamp 1
		.amdhsa_ieee_mode 1
		.amdhsa_fp16_overflow 0
		.amdhsa_tg_split 0
		.amdhsa_exception_fp_ieee_invalid_op 0
		.amdhsa_exception_fp_denorm_src 0
		.amdhsa_exception_fp_ieee_div_zero 0
		.amdhsa_exception_fp_ieee_overflow 0
		.amdhsa_exception_fp_ieee_underflow 0
		.amdhsa_exception_fp_ieee_inexact 0
		.amdhsa_exception_int_div_zero 0
	.end_amdhsa_kernel

amdhsa.kernels:
  - .agpr_count:     0
    .args:
      - .actual_access:  read_only
        .address_space:  global
        .offset:         0
        .size:           8
        .value_kind:     global_buffer
      - .actual_access:  read_only
        .address_space:  global
        .offset:         8
        .size:           8
        .value_kind:     global_buffer
      - .actual_access:  read_only
        .address_space:  global
        .offset:         16
        .size:           8
        .value_kind:     global_buffer
      - .actual_access:  read_only
        .address_space:  global
        .offset:         24
        .size:           8
        .value_kind:     global_buffer
      - .actual_access:  read_only
        .address_space:  global
        .offset:         32
        .size:           8
        .value_kind:     global_buffer
      - .actual_access:  read_only
        .address_space:  global
        .offset:         40
        .size:           8
        .value_kind:     global_buffer
      - .actual_access:  read_only
        .address_space:  global
        .offset:         48
        .size:           8
        .value_kind:     global_buffer
      - .actual_access:  write_only
        .address_space:  global
        .offset:         56
        .size:           8
        .value_kind:     global_buffer
    .group_segment_fixed_size: 98304
    .kernarg_segment_align: 8
    .kernarg_segment_size: 64
    .language:       OpenCL C
    .language_version:
      - 2
      - 0
    .max_flat_workgroup_size: 512
    .name:           _Z11k_conv_mfmaPKDF16_PKDv8_DF16_PKfS5_S5_S5_S5_PDF16_
    .private_segment_fixed_size: 0
    .sgpr_count:     36
    .sgpr_spill_count: 0
    .symbol:         _Z11k_conv_mfmaPKDF16_PKDv8_DF16_PKfS5_S5_S5_S5_PDF16_.kd
    .uniform_work_group_size: 1
    .uses_dynamic_stack: false
    .vgpr_count:     164
    .vgpr_spill_count: 0
    .wavefront_size: 64
  - .agpr_count:     0
    .args:
      - .actual_access:  read_only
        .address_space:  global
        .offset:         0
        .size:           8
        .value_kind:     global_buffer
      - .actual_access:  read_only
        .address_space:  global
        .offset:         8
        .size:           8
        .value_kind:     global_buffer
      - .actual_access:  read_only
        .address_space:  global
        .offset:         16
        .size:           8
        .value_kind:     global_buffer
      - .actual_access:  write_only
        .address_space:  global
        .offset:         24
        .size:           8
        .value_kind:     global_buffer
    .group_segment_fixed_size: 25600
    .kernarg_segment_align: 8
    .kernarg_segment_size: 32
    .language:       OpenCL C
    .language_version:
      - 2
      - 0
    .max_flat_workgroup_size: 1024
    .name:           _Z12k_recon_mfmaPKDF16_PKDv8_DF16_PKfPf
    .private_segment_fixed_size: 0
    .sgpr_count:     25
    .sgpr_spill_count: 0
    .symbol:         _Z12k_recon_mfmaPKDF16_PKDv8_DF16_PKfPf.kd
    .uniform_work_group_size: 1
    .uses_dynamic_stack: false
    .vgpr_count:     84
    .vgpr_spill_count: 0
    .wavefront_size: 64
  - .agpr_count:     0
    .args:
      - .actual_access:  read_only
        .address_space:  global
        .offset:         0
        .size:           8
        .value_kind:     global_buffer
      - .actual_access:  read_only
        .address_space:  global
        .offset:         8
        .size:           8
        .value_kind:     global_buffer
      - .actual_access:  read_only
        .address_space:  global
        .offset:         16
        .size:           8
        .value_kind:     global_buffer
      - .actual_access:  write_only
        .address_space:  global
        .offset:         24
        .size:           8
        .value_kind:     global_buffer
      - .actual_access:  write_only
        .address_space:  global
        .offset:         32
        .size:           8
        .value_kind:     global_buffer
      - .actual_access:  write_only
        .address_space:  global
        .offset:         40
        .size:           8
        .value_kind:     global_buffer
      - .actual_access:  write_only
        .address_space:  global
        .offset:         48
        .size:           8
        .value_kind:     global_buffer
      - .actual_access:  write_only
        .address_space:  global
        .offset:         56
        .size:           8
        .value_kind:     global_buffer
      - .actual_access:  write_only
        .address_space:  global
        .offset:         64
        .size:           8
        .value_kind:     global_buffer
    .group_segment_fixed_size: 67600
    .kernarg_segment_align: 8
    .kernarg_segment_size: 72
    .language:       OpenCL C
    .language_version:
      - 2
      - 0
    .max_flat_workgroup_size: 512
    .name:           _Z11k_proj_mfmaPKDF16_PKDv8_DF16_PKfPfPS1_S6_PhS6_PDF16_
    .private_segment_fixed_size: 0
    .sgpr_count:     36
    .sgpr_spill_count: 0
    .symbol:         _Z11k_proj_mfmaPKDF16_PKDv8_DF16_PKfPfPS1_S6_PhS6_PDF16_.kd
    .uniform_work_group_size: 1
    .uses_dynamic_stack: false
    .vgpr_count:     155
    .vgpr_spill_count: 0
    .wavefront_size: 64
  - .agpr_count:     0
    .args:
      - .actual_access:  read_only
        .address_space:  global
        .offset:         0
        .size:           8
        .value_kind:     global_buffer
      - .actual_access:  read_only
        .address_space:  global
        .offset:         8
        .size:           8
        .value_kind:     global_buffer
      - .actual_access:  read_only
        .address_space:  global
        .offset:         16
        .size:           8
        .value_kind:     global_buffer
      - .actual_access:  read_only
        .address_space:  global
        .offset:         24
        .size:           8
        .value_kind:     global_buffer
      - .actual_access:  read_only
        .address_space:  global
        .offset:         32
        .size:           8
        .value_kind:     global_buffer
      - .actual_access:  read_only
        .address_space:  global
        .offset:         40
        .size:           8
        .value_kind:     global_buffer
      - .actual_access:  write_only
        .address_space:  global
        .offset:         48
        .size:           8
        .value_kind:     global_buffer
      - .actual_access:  write_only
        .address_space:  global
        .offset:         56
        .size:           8
        .value_kind:     global_buffer
      - .actual_access:  read_only
        .address_space:  global
        .offset:         64
        .size:           8
        .value_kind:     global_buffer
      - .actual_access:  read_only
        .address_space:  global
        .offset:         72
        .size:           8
        .value_kind:     global_buffer
      - .actual_access:  write_only
        .address_space:  global
        .offset:         80
        .size:           8
        .value_kind:     global_buffer
      - .actual_access:  write_only
        .address_space:  global
        .offset:         88
        .size:           8
        .value_kind:     global_buffer
    .group_segment_fixed_size: 65536
    .kernarg_segment_align: 8
    .kernarg_segment_size: 96
    .language:       OpenCL C
    .language_version:
      - 2
      - 0
    .max_flat_workgroup_size: 512
    .name:           _Z6k_attnPKDv8_DF16_PKfPKhS3_S3_S3_PfS6_S3_S3_PS_S7_
    .private_segment_fixed_size: 0
    .sgpr_count:     34
    .sgpr_spill_count: 0
    .symbol:         _Z6k_attnPKDv8_DF16_PKfPKhS3_S3_S3_PfS6_S3_S3_PS_S7_.kd
    .uniform_work_group_size: 1
    .uses_dynamic_stack: false
    .vgpr_count:     126
    .vgpr_spill_count: 0
    .wavefront_size: 64
  - .agpr_count:     8
    .args:
      - .actual_access:  read_only
        .address_space:  global
        .offset:         0
        .size:           8
        .value_kind:     global_buffer
      - .actual_access:  read_only
        .address_space:  global
        .offset:         8
        .size:           8
        .value_kind:     global_buffer
      - .actual_access:  read_only
        .address_space:  global
        .offset:         16
        .size:           8
        .value_kind:     global_buffer
      - .actual_access:  read_only
        .address_space:  global
        .offset:         24
        .size:           8
        .value_kind:     global_buffer
      - .actual_access:  read_only
        .address_space:  global
        .offset:         32
        .size:           8
        .value_kind:     global_buffer
      - .actual_access:  write_only
        .address_space:  global
        .offset:         40
        .size:           8
        .value_kind:     global_buffer
    .group_segment_fixed_size: 10560
    .kernarg_segment_align: 8
    .kernarg_segment_size: 48
    .language:       OpenCL C
    .language_version:
      - 2
      - 0
    .max_flat_workgroup_size: 256
    .name:           _Z8k_resid2PKDF16_PKfS0_S2_S2_PDF16_
    .private_segment_fixed_size: 0
    .sgpr_count:     38
    .sgpr_spill_count: 0
    .symbol:         _Z8k_resid2PKDF16_PKfS0_S2_S2_PDF16_.kd
    .uniform_work_group_size: 1
    .uses_dynamic_stack: false
    .vgpr_count:     120
    .vgpr_spill_count: 0
    .wavefront_size: 64
  - .agpr_count:     0
    .args:
      - .actual_access:  read_only
        .address_space:  global
        .offset:         0
        .size:           8
        .value_kind:     global_buffer
      - .actual_access:  read_only
        .address_space:  global
        .offset:         8
        .size:           8
        .value_kind:     global_buffer
      - .actual_access:  read_only
        .address_space:  global
        .offset:         16
        .size:           8
        .value_kind:     global_buffer
      - .actual_access:  read_only
        .address_space:  global
        .offset:         24
        .size:           8
        .value_kind:     global_buffer
      - .actual_access:  read_only
        .address_space:  global
        .offset:         32
        .size:           8
        .value_kind:     global_buffer
      - .actual_access:  read_only
        .address_space:  global
        .offset:         40
        .size:           8
        .value_kind:     global_buffer
      - .actual_access:  read_only
        .address_space:  global
        .offset:         48
        .size:           8
        .value_kind:     global_buffer
      - .actual_access:  read_only
        .address_space:  global
        .offset:         56
        .size:           8
        .value_kind:     global_buffer
      - .actual_access:  read_only
        .address_space:  global
        .offset:         64
        .size:           8
        .value_kind:     global_buffer
      - .actual_access:  read_only
        .address_space:  global
        .offset:         72
        .size:           8
        .value_kind:     global_buffer
      - .actual_access:  write_only
        .address_space:  global
        .offset:         80
        .size:           8
        .value_kind:     global_buffer
      - .actual_access:  read_only
        .address_space:  global
        .offset:         88
        .size:           8
        .value_kind:     global_buffer
      - .actual_access:  read_only
        .address_space:  global
        .offset:         96
        .size:           8
        .value_kind:     global_buffer
      - .actual_access:  read_only
        .address_space:  global
        .offset:         104
        .size:           8
        .value_kind:     global_buffer
      - .actual_access:  read_only
        .address_space:  global
        .offset:         112
        .size:           8
        .value_kind:     global_buffer
      - .actual_access:  read_only
        .address_space:  global
        .offset:         120
        .size:           8
        .value_kind:     global_buffer
      - .actual_access:  read_only
        .address_space:  global
        .offset:         128
        .size:           8
        .value_kind:     global_buffer
      - .actual_access:  write_only
        .address_space:  global
        .offset:         136
        .size:           8
        .value_kind:     global_buffer
    .group_segment_fixed_size: 21248
    .kernarg_segment_align: 8
    .kernarg_segment_size: 144
    .language:       OpenCL C
    .language_version:
      - 2
      - 0
    .max_flat_workgroup_size: 512
    .name:           _Z8k_embed2PKfS0_S0_S0_S0_S0_S0_S0_S0_S0_PDF16_S0_S0_S0_S0_S0_S0_PDv8_DF16_
    .private_segment_fixed_size: 0
    .sgpr_count:     78
    .sgpr_spill_count: 0
    .symbol:         _Z8k_embed2PKfS0_S0_S0_S0_S0_S0_S0_S0_S0_PDF16_S0_S0_S0_S0_S0_S0_PDv8_DF16_.kd
    .uniform_work_group_size: 1
    .uses_dynamic_stack: false
    .vgpr_count:     99
    .vgpr_spill_count: 0
    .wavefront_size: 64
